# static s_setprio 1 for waves 4-7 during the MoE gate/up main K-loop
# speedup vs baseline: 1.0084x; 1.0084x over previous
.LBB0_1432:
	s_lshr_b32 s33, s2, 6
	s_lshl_b32 s3, s33, 1
	v_or_b32_e32 v2, s3, v193
	s_and_b32 s36, s33, 4
	s_and_b32 s37, s2, 0xc0
	v_and_or_b32 v3, v2, 3, s36
	s_lshr_b32 s36, s2, 1
	s_or_b32 s2, s37, 32
	v_bitop3_b32 v183, s2, v203, v198 bitop3:0xde
	s_or_b32 s2, s37, 0x100
	v_bitop3_b32 v181, s2, v203, v198 bitop3:0xde
	s_or_b32 s2, s37, 0x120
	s_lshl_b32 s38, s33, 10
	v_bitop3_b32 v172, s2, v203, v198 bitop3:0xde
	s_add_i32 s38, s38, 0
	s_mov_b32 s2, m0
	s_mov_b32 m0, s38
	s_nop 0
	global_load_lds_dwordx4 v34, s[18:19]
	s_mov_b32 m0, s2
	s_add_i32 s2, s38, 0x2000
	s_mov_b32 s39, m0
	s_mov_b32 m0, s2
	s_nop 0
	global_load_lds_dwordx4 v35, s[18:19]
	s_mov_b32 m0, s39
	s_add_i32 s2, s38, 0x4000
	s_mov_b32 s39, m0
	s_mov_b32 m0, s2
	s_nop 0
	global_load_lds_dwordx4 v36, s[18:19]
	s_mov_b32 m0, s39
	s_add_i32 s2, s38, 0x6000
	v_lshlrev_b32_e32 v2, 9, v2
	v_lshlrev_b32_e32 v3, 5, v3
	s_and_b32 s36, s36, 0x7fffff80
	s_mov_b32 s39, m0
	s_mov_b32 m0, s2
	s_nop 0
	global_load_lds_dwordx4 v37, s[18:19]
	s_mov_b32 m0, s39
	s_mul_i32 s2, s33, 0x5800
	v_bitop3_b32 v214, v3, v2, v194 bitop3:0xde
	v_or_b32_e32 v2, s36, v1
	s_mul_hi_u32 s39, s3, 0x2c00
	s_add_u32 s40, s59, s2
	s_waitcnt vmcnt(1)
	v_lshlrev_b32_e32 v38, 7, v2
	s_addc_u32 s41, s73, s39
	global_load_dwordx4 v[2:5], v199, s[40:41]
	s_add_i32 s40, s3, 16
	s_add_i32 s83, s2, 0x2c000
	s_mul_hi_u32 s84, s40, 0x2c00
	s_add_u32 s40, s59, s83
	s_addc_u32 s41, s73, s84
	global_load_dwordx4 v[6:9], v199, s[40:41]
	s_add_i32 s40, s3, 32
	s_add_i32 s85, s2, 0x58000
	s_mul_hi_u32 s86, s40, 0x2c00
	s_add_u32 s40, s59, s85
	s_addc_u32 s41, s73, s86
	global_load_dwordx4 v[10:13], v199, s[40:41]
	s_add_i32 s40, s3, 48
	s_add_i32 s87, s2, 0x84000
	s_mul_hi_u32 s88, s40, 0x2c00
	s_add_u32 s40, s59, s87
	s_addc_u32 s41, s73, s88
	global_load_dwordx4 v[14:17], v199, s[40:41]
	s_add_u32 s40, s74, s2
	s_addc_u32 s41, s75, s39
	global_load_dwordx4 v[18:21], v199, s[40:41]
	s_add_u32 s40, s74, s83
	s_addc_u32 s41, s75, s84
	global_load_dwordx4 v[22:25], v199, s[40:41]
	s_add_u32 s40, s74, s85
	s_addc_u32 s41, s75, s86
	global_load_dwordx4 v[26:29], v199, s[40:41]
	s_add_u32 s40, s74, s87
	s_addc_u32 s41, s75, s88
	global_load_dwordx4 v[30:33], v199, s[40:41]
	s_add_i32 s40, s38, 0x8000
	v_add_u32_e32 v39, 0x80, v34
	s_mov_b32 s41, m0
	s_mov_b32 m0, s40
	s_nop 0
	global_load_lds_dwordx4 v39, s[18:19]
	s_mov_b32 m0, s41
	v_add_u32_e32 v39, 0x80, v35
	s_add_i32 s40, s38, 0xa000
	s_mov_b32 s41, m0
	s_mov_b32 m0, s40
	s_nop 0
	global_load_lds_dwordx4 v39, s[18:19]
	s_mov_b32 m0, s41
	v_add_u32_e32 v39, 0x80, v36
	s_add_i32 s40, s38, 0xc000
	s_mov_b32 s41, m0
	s_mov_b32 m0, s40
	s_nop 0
	global_load_lds_dwordx4 v39, s[18:19]
	s_mov_b32 m0, s41
	v_add_u32_e32 v39, 0x80, v37
	s_add_i32 s40, s38, 0xe000
	s_mov_b32 s41, m0
	s_mov_b32 m0, s40
	s_nop 0
	global_load_lds_dwordx4 v39, s[18:19]
	s_mov_b32 m0, s41
	s_waitcnt vmcnt(4)
	v_add_u32_e32 v217, s52, v214
	v_cvt_pk_bf16_f32 v2, v2, v3
	v_cvt_pk_bf16_f32 v3, v4, v5
	v_cvt_pk_bf16_f32 v4, v6, v7
	v_cvt_pk_bf16_f32 v5, v8, v9
	v_or_b32_e32 v213, 0x100, v214
	ds_write2st64_b64 v217, v[2:3], v[4:5] offset1:16
	v_cvt_pk_bf16_f32 v2, v10, v11
	v_cvt_pk_bf16_f32 v3, v12, v13
	v_cvt_pk_bf16_f32 v4, v14, v15
	v_cvt_pk_bf16_f32 v5, v16, v17
	ds_write2st64_b64 v217, v[2:3], v[4:5] offset0:32 offset1:48
	v_cvt_pk_bf16_f32 v2, v18, v19
	v_cvt_pk_bf16_f32 v3, v20, v21
	v_add_u32_e32 v6, s52, v213
	v_cvt_pk_bf16_f32 v4, v22, v23
	v_cvt_pk_bf16_f32 v5, v24, v25
	s_add_i32 s40, s3, 64
	s_add_i32 s83, s2, 0xb0000
	ds_write2st64_b64 v6, v[2:3], v[4:5] offset1:16
	v_cvt_pk_bf16_f32 v2, v26, v27
	v_cvt_pk_bf16_f32 v3, v28, v29
	v_cvt_pk_bf16_f32 v4, v30, v31
	v_cvt_pk_bf16_f32 v5, v32, v33
	s_mul_hi_u32 s84, s40, 0x2c00
	s_add_u32 s40, s59, s83
	ds_write2st64_b64 v6, v[2:3], v[4:5] offset0:32 offset1:48
	s_addc_u32 s41, s73, s84
	global_load_dwordx4 v[30:33], v199, s[40:41]
	s_add_i32 s40, s3, 0x50
	s_add_i32 s85, s2, 0xdc000
	s_mul_hi_u32 s86, s40, 0x2c00
	s_add_u32 s40, s59, s85
	s_addc_u32 s41, s73, s86
	global_load_dwordx4 v[26:29], v199, s[40:41]
	s_add_i32 s40, s3, 0x60
	s_add_i32 s87, s2, 0x108000
	s_mul_hi_u32 s88, s40, 0x2c00
	s_add_u32 s40, s59, s87
	s_addc_u32 s41, s73, s88
	s_addk_i32 s3, 0x70
	s_add_i32 s89, s2, 0x134000
	global_load_dwordx4 v[22:25], v199, s[40:41]
	s_mul_hi_u32 s3, s3, 0x2c00
	s_add_u32 s40, s59, s89
	s_addc_u32 s41, s73, s3
	global_load_dwordx4 v[18:21], v199, s[40:41]
	s_add_u32 s40, s74, s83
	s_addc_u32 s41, s75, s84
	global_load_dwordx4 v[14:17], v199, s[40:41]
	s_add_u32 s40, s74, s85
	s_addc_u32 s41, s75, s86
	global_load_dwordx4 v[10:13], v199, s[40:41]
	s_add_u32 s40, s74, s87
	s_addc_u32 s41, s75, s88
	global_load_dwordx4 v[6:9], v199, s[40:41]
	s_add_u32 s40, s74, s89
	s_addc_u32 s41, s75, s3
	global_load_dwordx4 v[2:5], v199, s[40:41]
	s_mul_hi_u32 s3, s33, 0x5800
	s_add_u32 s40, s74, s2
	s_waitcnt lgkmcnt(0)
	s_barrier
	s_addc_u32 s41, s75, s3
	s_add_u32 s83, s59, s2
	v_add_u32_e32 v221, 0x100, v34
	v_mov_b32_e32 v34, 0
	v_bitop3_b32 v212, s37, v203, v198 bitop3:0xde
	v_or_b32_e32 v215, v38, v196
	s_mov_b32 s39, 0x8000
	v_or_b32_e32 v216, v38, v197
	s_addc_u32 s84, s73, s3
	v_add_u32_e32 v218, 0x100, v37
	v_add_u32_e32 v219, 0x100, v36
	v_add_u32_e32 v220, 0x100, v35
	s_mov_b32 s85, 0x10000
	s_mov_b32 s86, 0
	s_mov_b64 s[2:3], 0
	v_mov_b32_e32 v35, v34
	v_mov_b32_e32 v36, v34
	v_mov_b32_e32 v37, v34
	v_mov_b32_e32 v38, v34
	v_mov_b32_e32 v39, v34
	v_mov_b32_e32 v40, v34
	v_mov_b32_e32 v41, v34
	v_mov_b32_e32 v46, v34
	v_mov_b32_e32 v47, v34
	v_mov_b32_e32 v48, v34
	v_mov_b32_e32 v49, v34
	v_mov_b32_e32 v50, v34
	v_mov_b32_e32 v51, v34
	v_mov_b32_e32 v52, v34
	v_mov_b32_e32 v53, v34
	s_waitcnt vmcnt(0)
	v_mov_b32_e32 v42, v34
	v_mov_b32_e32 v43, v34
	v_mov_b32_e32 v44, v34
	v_mov_b32_e32 v45, v34
	v_mov_b32_e32 v54, v34
	v_mov_b32_e32 v55, v34
	v_mov_b32_e32 v56, v34
	v_mov_b32_e32 v57, v34
	v_mov_b32_e32 v58, v34
	v_mov_b32_e32 v59, v34
	v_mov_b32_e32 v60, v34
	v_mov_b32_e32 v61, v34
	v_mov_b32_e32 v62, v34
	v_mov_b32_e32 v63, v34
	v_mov_b32_e32 v64, v34
	v_mov_b32_e32 v65, v34
	v_mov_b32_e32 v66, v34
	v_mov_b32_e32 v67, v34
	v_mov_b32_e32 v68, v34
	v_mov_b32_e32 v69, v34
	v_mov_b32_e32 v70, v34
	v_mov_b32_e32 v71, v34
	v_mov_b32_e32 v72, v34
	v_mov_b32_e32 v73, v34
	v_mov_b32_e32 v74, v34
	v_mov_b32_e32 v75, v34
	v_mov_b32_e32 v76, v34
	v_mov_b32_e32 v77, v34
	v_mov_b32_e32 v78, v34
	v_mov_b32_e32 v79, v34
	v_mov_b32_e32 v80, v34
	v_mov_b32_e32 v81, v34
	v_mov_b32_e32 v82, v34
	v_mov_b32_e32 v83, v34
	v_mov_b32_e32 v84, v34
	v_mov_b32_e32 v85, v34
	v_mov_b32_e32 v86, v34
	v_mov_b32_e32 v87, v34
	v_mov_b32_e32 v88, v34
	v_mov_b32_e32 v89, v34
	v_mov_b32_e32 v90, v34
	v_mov_b32_e32 v91, v34
	v_mov_b32_e32 v92, v34
	v_mov_b32_e32 v93, v34
	v_mov_b32_e32 v94, v34
	v_mov_b32_e32 v95, v34
	v_mov_b32_e32 v96, v34
	v_mov_b32_e32 v97, v34
	v_mov_b32_e32 v98, v34
	v_mov_b32_e32 v99, v34
	v_mov_b32_e32 v100, v34
	v_mov_b32_e32 v101, v34
	v_mov_b32_e32 v102, v34
	v_mov_b32_e32 v103, v34
	v_mov_b32_e32 v104, v34
	v_mov_b32_e32 v105, v34
	v_mov_b32_e32 v106, v34
	v_mov_b32_e32 v107, v34
	v_mov_b32_e32 v108, v34
	v_mov_b32_e32 v109, v34
	v_mov_b32_e32 v110, v34
	v_mov_b32_e32 v111, v34
	v_mov_b32_e32 v112, v34
	v_mov_b32_e32 v113, v34
	v_mov_b32_e32 v114, v34
	v_mov_b32_e32 v115, v34
	v_mov_b32_e32 v116, v34
	v_mov_b32_e32 v117, v34
	v_mov_b32_e32 v118, v34
	v_mov_b32_e32 v119, v34
	v_mov_b32_e32 v120, v34
	v_mov_b32_e32 v121, v34
	v_mov_b32_e32 v122, v34
	v_mov_b32_e32 v123, v34
	v_mov_b32_e32 v124, v34
	v_mov_b32_e32 v125, v34
	v_mov_b32_e32 v126, v34
	v_mov_b32_e32 v127, v34
	v_mov_b32_e32 v128, v34
	v_mov_b32_e32 v129, v34
	v_mov_b32_e32 v130, v34
	v_mov_b32_e32 v131, v34
	v_mov_b32_e32 v132, v34
	v_mov_b32_e32 v133, v34
	v_mov_b32_e32 v134, v34
	v_mov_b32_e32 v135, v34
	v_mov_b32_e32 v136, v34
	v_mov_b32_e32 v137, v34
	v_mov_b32_e32 v138, v34
	v_mov_b32_e32 v139, v34
	v_mov_b32_e32 v140, v34
	v_mov_b32_e32 v141, v34
	v_mov_b32_e32 v142, v34
	v_mov_b32_e32 v143, v34
	v_mov_b32_e32 v144, v34
	v_mov_b32_e32 v145, v34
	v_mov_b32_e32 v146, v34
	v_mov_b32_e32 v147, v34
	v_mov_b32_e32 v148, v34
	v_mov_b32_e32 v149, v34
	v_mov_b32_e32 v150, v34
	v_mov_b32_e32 v151, v34
	v_mov_b32_e32 v152, v34
	v_mov_b32_e32 v153, v34
	v_mov_b32_e32 v154, v34
	v_mov_b32_e32 v155, v34
	v_mov_b32_e32 v156, v34
	v_mov_b32_e32 v157, v34
	v_mov_b32_e32 v158, v34
	v_mov_b32_e32 v159, v34
	v_mov_b32_e32 v160, v34
	v_mov_b32_e32 v161, v34
	s_cmp_lt_u32 s33, 4
	s_cbranch_scc1 .Lprio_m1
	s_setprio 1
.Lprio_m1:
.LBB0_1433:
	s_add_i32 s88, s39, 0xffff8000
	s_and_b32 s88, s88, 0x8000
	s_add_i32 s88, s88, 0
	s_add_i32 s87, s86, 0
	s_add_i32 s88, s88, 0x18000
	v_add_u32_e32 v246, s88, v212
	v_add_u32_e32 v247, s87, v215
	v_add_u32_e32 v252, s88, v181
	v_add_u32_e32 v254, s88, v172
	v_add_u32_e32 v250, s88, v183
	ds_read_b64_tr_b16 v[222:223], v246
	ds_read_b64_tr_b16 v[224:225], v246 offset:2048
	ds_read_b64_tr_b16 v[226:227], v250
	ds_read_b64_tr_b16 v[228:229], v250 offset:2048
	ds_read_b128 v[162:165], v247
	ds_read_b128 v[166:169], v247 offset:2048
	ds_read_b64_tr_b16 v[230:231], v252
	ds_read_b64_tr_b16 v[232:233], v252 offset:2048
	ds_read_b64_tr_b16 v[234:235], v254
	ds_read_b64_tr_b16 v[236:237], v254 offset:2048
	s_waitcnt lgkmcnt(5)
	v_mfma_f32_16x16x32_bf16 v[62:65], v[222:225], v[162:165], v[62:65]
	ds_read_b128 v[238:241], v247 offset:4096
	s_and_b32 s88, s39, 0x8000
	s_add_i32 s89, s38, s85
	v_mfma_f32_16x16x32_bf16 v[58:61], v[226:229], v[162:165], v[58:61]
	s_mov_b32 s90, m0
	s_mov_b32 m0, s89
	s_nop 0
	global_load_lds_dwordx4 v221, s[18:19]
	s_mov_b32 m0, s90
	s_waitcnt lgkmcnt(3)
	v_mfma_f32_16x16x32_bf16 v[54:57], v[230:233], v[162:165], v[54:57]
	s_waitcnt lgkmcnt(1)
	v_mfma_f32_16x16x32_bf16 v[42:45], v[234:237], v[162:165], v[42:45]
	v_mfma_f32_16x16x32_bf16 v[50:53], v[222:225], v[166:169], v[50:53]
	ds_read_b128 v[162:165], v247 offset:6144
	s_add_i32 s90, s89, 0x2000
	s_mov_b32 s91, m0
	s_mov_b32 m0, s90
	s_nop 0
	global_load_lds_dwordx4 v220, s[18:19]
	s_mov_b32 m0, s91
	v_mfma_f32_16x16x32_bf16 v[46:49], v[226:229], v[166:169], v[46:49]
	v_mfma_f32_16x16x32_bf16 v[38:41], v[230:233], v[166:169], v[38:41]
	v_mfma_f32_16x16x32_bf16 v[34:37], v[234:237], v[166:169], v[34:37]
	s_waitcnt lgkmcnt(1)
	v_mfma_f32_16x16x32_bf16 v[66:69], v[222:225], v[238:241], v[66:69]
	ds_read_b128 v[166:169], v247 offset:8192
	s_add_i32 s90, s89, 0x4000
	s_mov_b32 s91, m0
	s_mov_b32 m0, s90
	s_nop 0
	global_load_lds_dwordx4 v219, s[18:19]
	s_mov_b32 m0, s91
	v_mfma_f32_16x16x32_bf16 v[70:73], v[226:229], v[238:241], v[70:73]
	v_mfma_f32_16x16x32_bf16 v[74:77], v[230:233], v[238:241], v[74:77]
	v_mfma_f32_16x16x32_bf16 v[78:81], v[234:237], v[238:241], v[78:81]
	s_waitcnt lgkmcnt(1)
	v_mfma_f32_16x16x32_bf16 v[82:85], v[222:225], v[162:165], v[82:85]
	ds_read_b128 v[238:241], v247 offset:10240
	s_addk_i32 s89, 0x6000
	s_mov_b32 s90, m0
	s_mov_b32 m0, s89
	s_nop 0
	global_load_lds_dwordx4 v218, s[18:19]
	s_mov_b32 m0, s90
	v_mfma_f32_16x16x32_bf16 v[86:89], v[226:229], v[162:165], v[86:89]
	v_mfma_f32_16x16x32_bf16 v[90:93], v[230:233], v[162:165], v[90:93]
	v_mfma_f32_16x16x32_bf16 v[94:97], v[234:237], v[162:165], v[94:97]
	ds_read_b128 v[242:245], v247 offset:12288
	ds_read_b64_tr_b16 v[162:163], v246 offset:16384
	ds_read_b64_tr_b16 v[164:165], v246 offset:18432
	s_waitcnt lgkmcnt(4)
	v_mfma_f32_16x16x32_bf16 v[98:101], v[222:225], v[166:169], v[98:101]
	v_mfma_f32_16x16x32_bf16 v[102:105], v[226:229], v[166:169], v[102:105]
	v_mfma_f32_16x16x32_bf16 v[106:109], v[230:233], v[166:169], v[106:109]
	v_mfma_f32_16x16x32_bf16 v[110:113], v[234:237], v[166:169], v[110:113]
	ds_read_b128 v[246:249], v247 offset:14336
	ds_read_b64_tr_b16 v[166:167], v250 offset:16384
	ds_read_b64_tr_b16 v[168:169], v250 offset:18432
	s_waitcnt lgkmcnt(6)
	v_mfma_f32_16x16x32_bf16 v[114:117], v[222:225], v[238:241], v[114:117]
	v_mfma_f32_16x16x32_bf16 v[118:121], v[226:229], v[238:241], v[118:121]
	v_mfma_f32_16x16x32_bf16 v[122:125], v[230:233], v[238:241], v[122:125]
	v_mfma_f32_16x16x32_bf16 v[126:129], v[234:237], v[238:241], v[126:129]
	v_add_u32_e32 v200, s87, v216
	ds_read_b128 v[238:241], v200
	ds_read_b64_tr_b16 v[250:251], v252 offset:16384
	ds_read_b64_tr_b16 v[252:253], v252 offset:18432
	s_waitcnt lgkmcnt(8)
	v_mfma_f32_16x16x32_bf16 v[130:133], v[222:225], v[242:245], v[130:133]
	v_mfma_f32_16x16x32_bf16 v[134:137], v[226:229], v[242:245], v[134:137]
	v_mfma_f32_16x16x32_bf16 v[138:141], v[230:233], v[242:245], v[138:141]
	v_mfma_f32_16x16x32_bf16 v[142:145], v[234:237], v[242:245], v[142:145]
	s_waitcnt lgkmcnt(5)
	v_mfma_f32_16x16x32_bf16 v[146:149], v[222:225], v[246:249], v[146:149]
	v_mfma_f32_16x16x32_bf16 v[150:153], v[226:229], v[246:249], v[150:153]
	ds_read_b128 v[222:225], v200 offset:2048
	ds_read_b64_tr_b16 v[226:227], v254 offset:16384
	ds_read_b64_tr_b16 v[228:229], v254 offset:18432
	v_mfma_f32_16x16x32_bf16 v[154:157], v[230:233], v[246:249], v[154:157]
	v_mfma_f32_16x16x32_bf16 v[158:161], v[234:237], v[246:249], v[158:161]
	ds_read_b128 v[230:233], v200 offset:4096
	s_waitcnt lgkmcnt(6)
	v_mfma_f32_16x16x32_bf16 v[62:65], v[162:165], v[238:241], v[62:65]
	s_add_u32 s87, s83, s2
	s_waitcnt vmcnt(11)
	s_addc_u32 s90, s84, s3
	v_mfma_f32_16x16x32_bf16 v[58:61], v[166:169], v[238:241], v[58:61]
	v_cvt_pk_bf16_f32 v30, v30, v31
	v_cvt_pk_bf16_f32 v31, v32, v33
	v_add_u32_e32 v242, s88, v217
	s_waitcnt lgkmcnt(4)
	v_mfma_f32_16x16x32_bf16 v[54:57], v[250:253], v[238:241], v[54:57]
	s_add_u32 s88, s87, 0x160000
	ds_write_b64 v242, v[30:31]
	s_addc_u32 s89, s90, 0
	s_waitcnt lgkmcnt(2)
	v_mfma_f32_16x16x32_bf16 v[42:45], v[226:229], v[238:241], v[42:45]
	global_load_dwordx4 v[30:33], v199, s[88:89]
	v_mfma_f32_16x16x32_bf16 v[50:53], v[162:165], v[222:225], v[50:53]
	ds_read_b128 v[234:237], v200 offset:6144
	s_waitcnt vmcnt(11)
	s_add_u32 s88, s87, 0x18c000
	v_mfma_f32_16x16x32_bf16 v[46:49], v[166:169], v[222:225], v[46:49]
	v_cvt_pk_bf16_f32 v26, v26, v27
	v_cvt_pk_bf16_f32 v27, v28, v29
	ds_write_b64 v242, v[26:27] offset:8192
	v_mfma_f32_16x16x32_bf16 v[38:41], v[250:253], v[222:225], v[38:41]
	s_addc_u32 s89, s90, 0
	global_load_dwordx4 v[26:29], v199, s[88:89]
	v_mfma_f32_16x16x32_bf16 v[34:37], v[226:229], v[222:225], v[34:37]
	s_waitcnt lgkmcnt(3)
	v_mfma_f32_16x16x32_bf16 v[66:69], v[162:165], v[230:233], v[66:69]
	ds_read_b128 v[222:225], v200 offset:8192
	s_waitcnt vmcnt(11)
	s_add_u32 s88, s87, 0x1b8000
	v_mfma_f32_16x16x32_bf16 v[70:73], v[166:169], v[230:233], v[70:73]
	v_cvt_pk_bf16_f32 v22, v22, v23
	v_cvt_pk_bf16_f32 v23, v24, v25
	ds_write_b64 v242, v[22:23] offset:16384
	v_mfma_f32_16x16x32_bf16 v[74:77], v[250:253], v[230:233], v[74:77]
	s_addc_u32 s89, s90, 0
	global_load_dwordx4 v[22:25], v199, s[88:89]
	v_mfma_f32_16x16x32_bf16 v[78:81], v[226:229], v[230:233], v[78:81]
	s_waitcnt lgkmcnt(3)
	v_mfma_f32_16x16x32_bf16 v[82:85], v[162:165], v[234:237], v[82:85]
	ds_read_b128 v[230:233], v200 offset:10240
	s_waitcnt vmcnt(11)
	s_add_u32 s88, s87, 0x1e4000
	v_mfma_f32_16x16x32_bf16 v[86:89], v[166:169], v[234:237], v[86:89]
	v_cvt_pk_bf16_f32 v18, v18, v19
	v_cvt_pk_bf16_f32 v19, v20, v21
	ds_write_b64 v242, v[18:19] offset:24576
	v_mfma_f32_16x16x32_bf16 v[90:93], v[250:253], v[234:237], v[90:93]
	s_addc_u32 s89, s90, 0
	global_load_dwordx4 v[18:21], v199, s[88:89]
	v_mfma_f32_16x16x32_bf16 v[94:97], v[226:229], v[234:237], v[94:97]
	ds_read_b128 v[234:237], v200 offset:12288
	s_waitcnt lgkmcnt(4)
	v_mfma_f32_16x16x32_bf16 v[98:101], v[162:165], v[222:225], v[98:101]
	s_add_u32 s87, s40, s2
	s_waitcnt vmcnt(11)
	s_addc_u32 s90, s41, s3
	v_mfma_f32_16x16x32_bf16 v[102:105], v[166:169], v[222:225], v[102:105]
	v_cvt_pk_bf16_f32 v14, v14, v15
	v_cvt_pk_bf16_f32 v15, v16, v17
	s_add_u32 s88, s87, 0x160000
	v_mfma_f32_16x16x32_bf16 v[106:109], v[250:253], v[222:225], v[106:109]
	ds_write_b64 v242, v[14:15] offset:256
	s_addc_u32 s89, s90, 0
	global_load_dwordx4 v[14:17], v199, s[88:89]
	v_mfma_f32_16x16x32_bf16 v[110:113], v[226:229], v[222:225], v[110:113]
	s_waitcnt lgkmcnt(3)
	v_mfma_f32_16x16x32_bf16 v[114:117], v[162:165], v[230:233], v[114:117]
	ds_read_b128 v[222:225], v200 offset:14336
	s_waitcnt vmcnt(11)
	s_add_u32 s88, s87, 0x18c000
	v_mfma_f32_16x16x32_bf16 v[118:121], v[166:169], v[230:233], v[118:121]
	v_cvt_pk_bf16_f32 v10, v10, v11
	v_cvt_pk_bf16_f32 v11, v12, v13
	ds_write_b64 v242, v[10:11] offset:8448
	v_mfma_f32_16x16x32_bf16 v[122:125], v[250:253], v[230:233], v[122:125]
	s_addc_u32 s89, s90, 0
	global_load_dwordx4 v[10:13], v199, s[88:89]
	v_mfma_f32_16x16x32_bf16 v[126:129], v[226:229], v[230:233], v[126:129]
	s_waitcnt lgkmcnt(3)
	v_mfma_f32_16x16x32_bf16 v[130:133], v[162:165], v[234:237], v[130:133]
	s_waitcnt vmcnt(11)
	s_add_u32 s88, s87, 0x1b8000
	v_cvt_pk_bf16_f32 v6, v6, v7
	v_mfma_f32_16x16x32_bf16 v[134:137], v[166:169], v[234:237], v[134:137]
	v_cvt_pk_bf16_f32 v7, v8, v9
	ds_write_b64 v242, v[6:7] offset:16640
	s_addc_u32 s89, s90, 0
	v_mfma_f32_16x16x32_bf16 v[138:141], v[250:253], v[234:237], v[138:141]
	global_load_dwordx4 v[6:9], v199, s[88:89]
	v_mfma_f32_16x16x32_bf16 v[142:145], v[226:229], v[234:237], v[142:145]
	s_waitcnt lgkmcnt(2)
	v_mfma_f32_16x16x32_bf16 v[146:149], v[162:165], v[222:225], v[146:149]
	s_waitcnt vmcnt(11)
	s_add_u32 s88, s87, 0x1e4000
	v_cvt_pk_bf16_f32 v2, v2, v3
	v_mfma_f32_16x16x32_bf16 v[150:153], v[166:169], v[222:225], v[150:153]
	v_cvt_pk_bf16_f32 v3, v4, v5
	ds_write_b64 v242, v[2:3] offset:24832
	s_addc_u32 s89, s90, 0
	v_mfma_f32_16x16x32_bf16 v[154:157], v[250:253], v[222:225], v[154:157]
	global_load_dwordx4 v[2:5], v199, s[88:89]
	v_mfma_f32_16x16x32_bf16 v[158:161], v[226:229], v[222:225], v[158:161]
	s_add_i32 s87, s86, 0x8000
	s_cmp_lg_u32 s86, 0x10000
	s_cselect_b32 s86, s87, 0
	s_add_i32 s87, s85, 0x8000
	s_cmp_lg_u32 s85, 0x10000
	s_waitcnt lgkmcnt(0)
	s_barrier
	s_cselect_b32 s85, s87, 0
	s_add_u32 s2, s2, 0xb0000
	s_addc_u32 s3, s3, 0
	s_add_i32 s39, s39, 0x8000
	v_add_u32_e32 v218, 0x80, v218
	v_add_u32_e32 v219, 0x80, v219
	v_add_u32_e32 v220, 0x80, v220
	s_cmp_lg_u32 s2, 0x14a0000
	v_add_u32_e32 v221, 0x80, v221
	s_cbranch_scc1 .LBB0_1433
	s_setprio 0
	v_add_u32_e32 v200, s52, v212
	v_add_u32_e32 v250, 0, v215
	v_add_u32_e32 v215, s52, v181
	v_add_u32_e32 v251, s52, v172
	v_add_u32_e32 v217, s52, v183
	ds_read_b64_tr_b16 v[162:163], v200
	ds_read_b64_tr_b16 v[164:165], v200 offset:2048
	ds_read_b64_tr_b16 v[166:167], v217
	ds_read_b64_tr_b16 v[168:169], v217 offset:2048
	ds_read_b128 v[218:221], v250
	ds_read_b128 v[222:225], v250 offset:2048
	ds_read_b64_tr_b16 v[226:227], v215
	ds_read_b64_tr_b16 v[228:229], v215 offset:2048
	ds_read_b64_tr_b16 v[230:231], v251
	ds_read_b64_tr_b16 v[232:233], v251 offset:2048
	s_waitcnt lgkmcnt(5)
	v_mfma_f32_16x16x32_bf16 v[62:65], v[162:165], v[218:221], v[62:65]
	ds_read_b128 v[234:237], v250 offset:4096
	v_mfma_f32_16x16x32_bf16 v[58:61], v[166:169], v[218:221], v[58:61]
	s_waitcnt lgkmcnt(3)
	v_mfma_f32_16x16x32_bf16 v[54:57], v[226:229], v[218:221], v[54:57]
	s_waitcnt lgkmcnt(1)
	v_mfma_f32_16x16x32_bf16 v[42:45], v[230:233], v[218:221], v[42:45]
	v_mfma_f32_16x16x32_bf16 v[50:53], v[162:165], v[222:225], v[50:53]
	ds_read_b128 v[218:221], v250 offset:6144
	v_mfma_f32_16x16x32_bf16 v[46:49], v[166:169], v[222:225], v[46:49]
	v_mfma_f32_16x16x32_bf16 v[38:41], v[226:229], v[222:225], v[38:41]
	v_mfma_f32_16x16x32_bf16 v[34:37], v[230:233], v[222:225], v[34:37]
	s_waitcnt lgkmcnt(1)
	v_mfma_f32_16x16x32_bf16 v[66:69], v[162:165], v[234:237], v[66:69]
	ds_read_b128 v[222:225], v250 offset:8192
	v_mfma_f32_16x16x32_bf16 v[70:73], v[166:169], v[234:237], v[70:73]
	v_mfma_f32_16x16x32_bf16 v[74:77], v[226:229], v[234:237], v[74:77]
	v_mfma_f32_16x16x32_bf16 v[78:81], v[230:233], v[234:237], v[78:81]
	s_waitcnt lgkmcnt(1)
	v_mfma_f32_16x16x32_bf16 v[82:85], v[162:165], v[218:221], v[82:85]
	ds_read_b128 v[234:237], v250 offset:10240
	v_mfma_f32_16x16x32_bf16 v[86:89], v[166:169], v[218:221], v[86:89]
	v_mfma_f32_16x16x32_bf16 v[90:93], v[226:229], v[218:221], v[90:93]
	v_mfma_f32_16x16x32_bf16 v[94:97], v[230:233], v[218:221], v[94:97]
	ds_read_b128 v[218:221], v250 offset:12288
	ds_read_b64_tr_b16 v[238:239], v200 offset:16384
	ds_read_b64_tr_b16 v[240:241], v200 offset:18432
	s_waitcnt lgkmcnt(4)
	v_mfma_f32_16x16x32_bf16 v[98:101], v[162:165], v[222:225], v[98:101]
	v_mfma_f32_16x16x32_bf16 v[102:105], v[166:169], v[222:225], v[102:105]
	v_mfma_f32_16x16x32_bf16 v[106:109], v[226:229], v[222:225], v[106:109]
	v_mfma_f32_16x16x32_bf16 v[110:113], v[230:233], v[222:225], v[110:113]
	ds_read_b128 v[222:225], v250 offset:14336
	ds_read_b64_tr_b16 v[242:243], v217 offset:16384
	ds_read_b64_tr_b16 v[244:245], v217 offset:18432
	s_waitcnt lgkmcnt(6)
	v_mfma_f32_16x16x32_bf16 v[114:117], v[162:165], v[234:237], v[114:117]
	v_mfma_f32_16x16x32_bf16 v[118:121], v[166:169], v[234:237], v[118:121]
	v_mfma_f32_16x16x32_bf16 v[122:125], v[226:229], v[234:237], v[122:125]
	v_mfma_f32_16x16x32_bf16 v[126:129], v[230:233], v[234:237], v[126:129]
	v_add_u32_e32 v200, 0, v216
	ds_read_b128 v[234:237], v200
	ds_read_b64_tr_b16 v[246:247], v215 offset:16384
	ds_read_b64_tr_b16 v[248:249], v215 offset:18432
	s_waitcnt lgkmcnt(8)
	v_mfma_f32_16x16x32_bf16 v[130:133], v[162:165], v[218:221], v[130:133]
	v_mfma_f32_16x16x32_bf16 v[134:137], v[166:169], v[218:221], v[134:137]
	v_mfma_f32_16x16x32_bf16 v[138:141], v[226:229], v[218:221], v[138:141]
	v_mfma_f32_16x16x32_bf16 v[142:145], v[230:233], v[218:221], v[142:145]
	s_waitcnt lgkmcnt(5)
	v_mfma_f32_16x16x32_bf16 v[146:149], v[162:165], v[222:225], v[146:149]
	v_mfma_f32_16x16x32_bf16 v[150:153], v[166:169], v[222:225], v[150:153]
	ds_read_b128 v[162:165], v200 offset:2048
	ds_read_b64_tr_b16 v[166:167], v251 offset:16384
	ds_read_b64_tr_b16 v[168:169], v251 offset:18432
	v_mfma_f32_16x16x32_bf16 v[154:157], v[226:229], v[222:225], v[154:157]
	v_mfma_f32_16x16x32_bf16 v[158:161], v[230:233], v[222:225], v[158:161]
	ds_read_b128 v[216:219], v200 offset:4096
	s_waitcnt vmcnt(7)
	v_add_u32_e32 v214, s56, v214
	v_cvt_pk_bf16_f32 v30, v30, v31
	v_cvt_pk_bf16_f32 v31, v32, v33
	s_waitcnt lgkmcnt(6)
	v_mfma_f32_16x16x32_bf16 v[62:65], v[238:241], v[234:237], v[62:65]
	ds_write_b64 v214, v[30:31]
	v_mfma_f32_16x16x32_bf16 v[58:61], v[242:245], v[234:237], v[58:61]
	s_waitcnt lgkmcnt(5)
	v_mfma_f32_16x16x32_bf16 v[54:57], v[246:249], v[234:237], v[54:57]
	s_waitcnt lgkmcnt(2)
	v_mfma_f32_16x16x32_bf16 v[30:33], v[166:169], v[234:237], v[42:45]
	v_mfma_f32_16x16x32_bf16 v[42:45], v[238:241], v[162:165], v[50:53]
	s_nop 2
	ds_read_b128 v[50:53], v200 offset:6144
	s_waitcnt vmcnt(6)
	v_mfma_f32_16x16x32_bf16 v[46:49], v[242:245], v[162:165], v[46:49]
	v_cvt_pk_bf16_f32 v26, v26, v27
	v_cvt_pk_bf16_f32 v27, v28, v29
	ds_write_b64 v214, v[26:27] offset:8192
	v_mfma_f32_16x16x32_bf16 v[38:41], v[246:249], v[162:165], v[38:41]
	v_mfma_f32_16x16x32_bf16 v[26:29], v[166:169], v[162:165], v[34:37]
	s_waitcnt lgkmcnt(3)
	v_mfma_f32_16x16x32_bf16 v[34:37], v[238:241], v[216:219], v[66:69]
	v_mfma_f32_16x16x32_bf16 v[66:69], v[242:245], v[216:219], v[70:73]
	s_nop 2
	ds_read_b128 v[70:73], v200 offset:8192
	s_waitcnt vmcnt(5)
	v_mfma_f32_16x16x32_bf16 v[74:77], v[246:249], v[216:219], v[74:77]
	v_cvt_pk_bf16_f32 v22, v22, v23
	v_cvt_pk_bf16_f32 v23, v24, v25
	ds_write_b64 v214, v[22:23] offset:16384
	v_mfma_f32_16x16x32_bf16 v[22:25], v[166:169], v[216:219], v[78:81]
	s_waitcnt lgkmcnt(3)
	v_mfma_f32_16x16x32_bf16 v[78:81], v[238:241], v[50:53], v[82:85]
	v_mfma_f32_16x16x32_bf16 v[82:85], v[242:245], v[50:53], v[86:89]
	s_nop 2
	ds_read_b128 v[86:89], v200 offset:10240
	s_waitcnt vmcnt(4)
	v_mfma_f32_16x16x32_bf16 v[90:93], v[246:249], v[50:53], v[90:93]
	v_cvt_pk_bf16_f32 v18, v18, v19
	v_cvt_pk_bf16_f32 v19, v20, v21
	ds_write_b64 v214, v[18:19] offset:24576
	v_mfma_f32_16x16x32_bf16 v[18:21], v[166:169], v[50:53], v[94:97]
	s_waitcnt lgkmcnt(3)
	v_mfma_f32_16x16x32_bf16 v[50:53], v[238:241], v[70:73], v[98:101]
	v_add_u32_e32 v162, s56, v213
	s_nop 1
	ds_read_b128 v[98:101], v200 offset:12288
	s_waitcnt vmcnt(3)
	v_mfma_f32_16x16x32_bf16 v[94:97], v[242:245], v[70:73], v[102:105]
	v_cvt_pk_bf16_f32 v14, v14, v15
	v_cvt_pk_bf16_f32 v15, v16, v17
	ds_write_b64 v162, v[14:15]
	v_mfma_f32_16x16x32_bf16 v[102:105], v[246:249], v[70:73], v[106:109]
	v_mfma_f32_16x16x32_bf16 v[14:17], v[166:169], v[70:73], v[110:113]
	s_nop 2
	ds_read_b128 v[110:113], v200 offset:14336
	s_waitcnt vmcnt(2)
	s_waitcnt lgkmcnt(4)
	v_mfma_f32_16x16x32_bf16 v[70:73], v[238:241], v[86:89], v[114:117]
	v_cvt_pk_bf16_f32 v10, v10, v11
	v_cvt_pk_bf16_f32 v11, v12, v13
	ds_write_b64 v162, v[10:11] offset:8192
	v_mfma_f32_16x16x32_bf16 v[106:109], v[242:245], v[86:89], v[118:121]
	v_mfma_f32_16x16x32_bf16 v[114:117], v[246:249], v[86:89], v[122:125]
	v_mfma_f32_16x16x32_bf16 v[10:13], v[166:169], v[86:89], v[126:129]
	s_waitcnt vmcnt(1)
	s_waitcnt lgkmcnt(3)
	v_mfma_f32_16x16x32_bf16 v[86:89], v[238:241], v[98:101], v[130:133]
	v_cvt_pk_bf16_f32 v6, v6, v7
	v_cvt_pk_bf16_f32 v7, v8, v9
	ds_write_b64 v162, v[6:7] offset:16384
	v_mfma_f32_16x16x32_bf16 v[118:121], v[242:245], v[98:101], v[134:137]
	v_mfma_f32_16x16x32_bf16 v[122:125], v[246:249], v[98:101], v[138:141]
	v_mfma_f32_16x16x32_bf16 v[6:9], v[166:169], v[98:101], v[142:145]
	s_waitcnt vmcnt(0)
	s_waitcnt lgkmcnt(2)
	v_mfma_f32_16x16x32_bf16 v[98:101], v[238:241], v[110:113], v[146:149]
	v_cvt_pk_bf16_f32 v2, v2, v3
	v_cvt_pk_bf16_f32 v3, v4, v5
	ds_write_b64 v162, v[2:3] offset:24576
	v_mfma_f32_16x16x32_bf16 v[126:129], v[242:245], v[110:113], v[150:153]
	v_mfma_f32_16x16x32_bf16 v[130:133], v[246:249], v[110:113], v[154:157]
	v_mfma_f32_16x16x32_bf16 v[2:5], v[166:169], v[110:113], v[158:161]
	s_waitcnt lgkmcnt(0)
	s_barrier
	v_add_u32_e32 v168, s56, v212
	v_add_u32_e32 v183, s56, v183
	v_add_u32_e32 v181, s56, v181
	ds_read_b64_tr_b16 v[110:111], v168
	ds_read_b64_tr_b16 v[112:113], v168 offset:2048
	ds_read_b64_tr_b16 v[134:135], v183
	ds_read_b64_tr_b16 v[136:137], v183 offset:2048
	ds_read_b128 v[138:141], v250 offset:32768
	ds_read_b64_tr_b16 v[142:143], v181
	ds_read_b128 v[146:149], v250 offset:34816
	ds_read_b128 v[150:153], v250 offset:36864
	ds_read_b64_tr_b16 v[144:145], v181 offset:2048
	v_add_u32_e32 v172, s56, v172
	ds_read_b64_tr_b16 v[154:155], v172
	ds_read_b64_tr_b16 v[156:157], v172 offset:2048
	s_waitcnt lgkmcnt(6)
	v_mfma_f32_16x16x32_bf16 v[62:65], v[110:113], v[138:141], v[62:65]
	v_mfma_f32_16x16x32_bf16 v[58:61], v[134:137], v[138:141], v[58:61]
	s_waitcnt lgkmcnt(2)
	v_mfma_f32_16x16x32_bf16 v[54:57], v[142:145], v[138:141], v[54:57]
	s_waitcnt lgkmcnt(0)
	v_mfma_f32_16x16x32_bf16 v[30:33], v[154:157], v[138:141], v[30:33]
	v_mfma_f32_16x16x32_bf16 v[42:45], v[110:113], v[146:149], v[42:45]
	ds_read_b128 v[138:141], v250 offset:38912
	v_mfma_f32_16x16x32_bf16 v[46:49], v[134:137], v[146:149], v[46:49]
	v_mfma_f32_16x16x32_bf16 v[38:41], v[142:145], v[146:149], v[38:41]
	v_mfma_f32_16x16x32_bf16 v[26:29], v[154:157], v[146:149], v[26:29]
	v_mfma_f32_16x16x32_bf16 v[34:37], v[110:113], v[150:153], v[34:37]
	ds_read_b128 v[146:149], v250 offset:40960
	v_mfma_f32_16x16x32_bf16 v[66:69], v[134:137], v[150:153], v[66:69]
	v_mfma_f32_16x16x32_bf16 v[74:77], v[142:145], v[150:153], v[74:77]
	v_mfma_f32_16x16x32_bf16 v[22:25], v[154:157], v[150:153], v[22:25]
	s_waitcnt lgkmcnt(1)
	v_mfma_f32_16x16x32_bf16 v[150:153], v[134:137], v[138:141], v[82:85]
	s_nop 2
	ds_read_b128 v[82:85], v250 offset:43008
	v_mfma_f32_16x16x32_bf16 v[78:81], v[110:113], v[138:141], v[78:81]
	v_mfma_f32_16x16x32_bf16 v[18:21], v[154:157], v[138:141], v[18:21]
	v_mfma_f32_16x16x32_bf16 v[158:161], v[142:145], v[138:141], v[90:93]
	s_nop 2
	ds_read_b128 v[90:93], v250 offset:45056
	ds_read_b64_tr_b16 v[166:167], v168 offset:16384
	ds_read_b64_tr_b16 v[168:169], v168 offset:18432
	s_waitcnt lgkmcnt(4)
	v_mfma_f32_16x16x32_bf16 v[50:53], v[110:113], v[146:149], v[50:53]
	v_mfma_f32_16x16x32_bf16 v[14:17], v[154:157], v[146:149], v[14:17]
	v_mfma_f32_16x16x32_bf16 v[138:141], v[134:137], v[146:149], v[94:97]
	v_mfma_f32_16x16x32_bf16 v[162:165], v[142:145], v[146:149], v[102:105]
	s_waitcnt lgkmcnt(3)
	v_mfma_f32_16x16x32_bf16 v[146:149], v[110:113], v[82:85], v[70:73]
	s_nop 2
	ds_read_b128 v[70:73], v250 offset:47104
	ds_read_b64_tr_b16 v[220:221], v183 offset:16384
	ds_read_b64_tr_b16 v[222:223], v183 offset:18432
	v_mfma_f32_16x16x32_bf16 v[10:13], v[154:157], v[82:85], v[10:13]
	v_mfma_f32_16x16x32_bf16 v[212:215], v[134:137], v[82:85], v[106:109]
	v_mfma_f32_16x16x32_bf16 v[216:219], v[142:145], v[82:85], v[114:117]
	ds_read_b128 v[82:85], v200 offset:32768
	ds_read_b64_tr_b16 v[236:237], v181 offset:16384
	ds_read_b64_tr_b16 v[238:239], v181 offset:18432
	s_waitcnt lgkmcnt(8)
	v_mfma_f32_16x16x32_bf16 v[6:9], v[154:157], v[90:93], v[6:9]
	v_mfma_f32_16x16x32_bf16 v[224:227], v[110:113], v[90:93], v[86:89]
	v_mfma_f32_16x16x32_bf16 v[228:231], v[134:137], v[90:93], v[118:121]
	v_mfma_f32_16x16x32_bf16 v[232:235], v[142:145], v[90:93], v[122:125]
	s_waitcnt lgkmcnt(5)
	v_mfma_f32_16x16x32_bf16 v[130:133], v[142:145], v[70:73], v[130:133]
	ds_read_b128 v[86:89], v200 offset:34816
	ds_read_b64_tr_b16 v[142:143], v172 offset:16384
	ds_read_b64_tr_b16 v[144:145], v172 offset:18432
	v_mfma_f32_16x16x32_bf16 v[240:243], v[110:113], v[70:73], v[98:101]
	v_mfma_f32_16x16x32_bf16 v[134:137], v[134:137], v[70:73], v[126:129]
	v_mfma_f32_16x16x32_bf16 v[154:157], v[154:157], v[70:73], v[2:5]
	s_nop 2
	ds_read_b128 v[2:5], v200 offset:36864
	s_waitcnt lgkmcnt(6)
	v_mfma_f32_16x16x32_bf16 v[122:125], v[166:169], v[82:85], v[62:65]
	v_mfma_f32_16x16x32_bf16 v[114:117], v[220:223], v[82:85], v[58:61]
	s_waitcnt lgkmcnt(4)
	v_mfma_f32_16x16x32_bf16 v[126:129], v[236:239], v[82:85], v[54:57]
	s_waitcnt lgkmcnt(1)
	v_mfma_f32_16x16x32_bf16 v[118:121], v[142:145], v[82:85], v[30:33]
	s_nop 2
	ds_read_b128 v[30:33], v200 offset:38912
	v_mfma_f32_16x16x32_bf16 v[106:109], v[166:169], v[86:89], v[42:45]
	v_mfma_f32_16x16x32_bf16 v[98:101], v[220:223], v[86:89], v[46:49]
	v_mfma_f32_16x16x32_bf16 v[110:113], v[236:239], v[86:89], v[38:41]
	v_mfma_f32_16x16x32_bf16 v[102:105], v[142:145], v[86:89], v[26:29]
	s_nop 2
	ds_read_b128 v[26:29], v200 offset:40960
	s_waitcnt lgkmcnt(2)
	v_mfma_f32_16x16x32_bf16 v[90:93], v[166:169], v[2:5], v[34:37]
	v_mfma_f32_16x16x32_bf16 v[82:85], v[220:223], v[2:5], v[66:69]
	v_mfma_f32_16x16x32_bf16 v[94:97], v[236:239], v[2:5], v[74:77]
	v_mfma_f32_16x16x32_bf16 v[86:89], v[142:145], v[2:5], v[22:25]
	ds_read_b128 v[2:5], v200 offset:43008
	s_waitcnt lgkmcnt(2)
	v_mfma_f32_16x16x32_bf16 v[74:77], v[166:169], v[30:33], v[78:81]
	v_mfma_f32_16x16x32_bf16 v[66:69], v[220:223], v[30:33], v[150:153]
	v_mfma_f32_16x16x32_bf16 v[78:81], v[236:239], v[30:33], v[158:161]
	v_mfma_f32_16x16x32_bf16 v[70:73], v[142:145], v[30:33], v[18:21]
	ds_read_b128 v[22:25], v200 offset:45056
	s_waitcnt lgkmcnt(2)
	v_mfma_f32_16x16x32_bf16 v[58:61], v[166:169], v[26:29], v[50:53]
	v_mfma_f32_16x16x32_bf16 v[50:53], v[220:223], v[26:29], v[138:141]
	v_mfma_f32_16x16x32_bf16 v[62:65], v[236:239], v[26:29], v[162:165]
	v_mfma_f32_16x16x32_bf16 v[54:57], v[142:145], v[26:29], v[14:17]
	s_waitcnt lgkmcnt(1)
	v_mfma_f32_16x16x32_bf16 v[42:45], v[166:169], v[2:5], v[146:149]
	ds_read_b128 v[138:141], v200 offset:47104
	v_mfma_f32_16x16x32_bf16 v[34:37], v[220:223], v[2:5], v[212:215]
	v_mfma_f32_16x16x32_bf16 v[46:49], v[236:239], v[2:5], v[216:219]
	v_mfma_f32_16x16x32_bf16 v[38:41], v[142:145], v[2:5], v[10:13]
	s_waitcnt lgkmcnt(1)
	v_mfma_f32_16x16x32_bf16 v[26:29], v[166:169], v[22:25], v[224:227]
	v_mfma_f32_16x16x32_bf16 v[18:21], v[220:223], v[22:25], v[228:231]
	v_mfma_f32_16x16x32_bf16 v[30:33], v[236:239], v[22:25], v[232:235]
	v_mfma_f32_16x16x32_bf16 v[22:25], v[142:145], v[22:25], v[6:9]
	s_waitcnt lgkmcnt(0)
	v_mfma_f32_16x16x32_bf16 v[10:13], v[166:169], v[138:141], v[240:243]
	v_mfma_f32_16x16x32_bf16 v[2:5], v[220:223], v[138:141], v[134:137]
	v_mfma_f32_16x16x32_bf16 v[14:17], v[236:239], v[138:141], v[130:133]
	v_mfma_f32_16x16x32_bf16 v[6:9], v[142:145], v[138:141], v[154:157]
	s_waitcnt lgkmcnt(0)
	s_barrier
	s_nop 0
	v_mov_b32_e32 v130, 0
	s_and_b64 vcc, exec, s[6:7]
	v_mov_b32_e32 v131, 0
	v_mov_b32_e32 v132, 0
	s_cbranch_vccnz .LBB0_1436
	global_load_dword v130, v[184:185], off
	global_load_dword v131, v[186:187], off
	global_load_dword v132, v[188:189], off
